# speedup vs baseline: 1.0048x; 1.0008x over previous
.LBB2_5:
	v_exp_f32_e32 v69, v46
	v_exp_f32_e32 v71, v47
	v_exp_f32_e32 v80, v42
	v_exp_f32_e32 v102, v43
	v_exp_f32_e32 v46, v44
	v_exp_f32_e32 v47, v45
	ds_read_b128 v[42:45], v114 offset:8192
	v_exp_f32_e32 v73, v48
	v_exp_f32_e32 v75, v49
	v_exp_f32_e32 v106, v38
	v_exp_f32_e32 v107, v39
	v_exp_f32_e32 v109, v40
	v_exp_f32_e32 v110, v41
	v_cvt_pk_f16_f32 v41, v46, v47
	v_cvt_pk_f16_f32 v40, v80, v102
	v_cvt_pk_f16_f32 v39, v73, v75
	v_cvt_pk_f16_f32 v38, v69, v71
	ds_read_b128 v[46:49], v114 offset:10240
	ds_read_b128 v[102:105], v114 offset:12288
	s_setprio 2
	s_waitcnt lgkmcnt(0)
	v_mfma_f32_16x16x32_f16 v[26:29], v[42:45], v[38:41], v[26:29]
	ds_read_b128 v[42:45], v114 offset:14336
	v_exp_f32_e32 v34, v34
	v_mfma_f32_16x16x32_f16 v[22:25], v[46:49], v[38:41], v[22:25]
	ds_read_b128 v[46:49], v115 offset:8192
	v_exp_f32_e32 v36, v36
	v_exp_f32_e32 v37, v37
	s_waitcnt lgkmcnt(0)
	v_mfma_f32_16x16x32_f16 v[10:13], v[42:45], v[38:41], v[10:13]
	ds_read_b128 v[42:45], v115 offset:12288
	v_exp_f32_e32 v35, v35
	v_cvt_pk_f16_f32 v37, v36, v37
	v_mfma_f32_16x16x32_f16 v[18:21], v[102:105], v[38:41], v[18:21]
	s_nop 0
	v_cvt_pk_f16_f32 v36, v34, v35
	v_cvt_pk_f16_f32 v35, v109, v110
	v_cvt_pk_f16_f32 v34, v106, v107
	s_mov_b64 s[38:39], 0
	ds_read_b128 v[102:105], v115 offset:10240
	v_mfma_f32_16x16x32_f16 v[26:29], v[46:49], v[34:37], v[26:29]
	ds_read_b128 v[46:49], v115 offset:14336
	s_waitcnt lgkmcnt(0)
	v_mfma_f32_16x16x32_f16 v[18:21], v[42:45], v[34:37], v[18:21]
	v_mfma_f32_16x16x32_f16 v[22:25], v[102:105], v[34:37], v[22:25]
	v_mfma_f32_16x16x32_f16 v[14:17], v[116:119], v[38:41], v[14:17]
	v_mfma_f32_16x16x32_f16 v[10:13], v[46:49], v[34:37], v[10:13]
	v_mfma_f32_16x16x32_f16 v[14:17], v[116:119], v[34:37], v[14:17]
	s_setprio 0

.Lattn_no_dma:
	s_add_i32 s48, s66, s64
	s_cmp_lg_u32 s48, 1
	s_setprio 2
	s_waitcnt lgkmcnt(4)
	v_mfma_f32_16x16x32_f16 v[34:37], v[34:37], v[6:9], v[30:33]
	s_waitcnt lgkmcnt(2)
	v_mfma_f32_16x16x32_f16 v[102:105], v[42:45], v[6:9], v[30:33]
	ds_read_b128 v[42:45], v115
	v_mfma_f32_16x16x32_f16 v[38:41], v[38:41], v[6:9], v[30:33]
	s_waitcnt lgkmcnt(1)
	v_mfma_f32_16x16x32_f16 v[106:109], v[46:49], v[6:9], v[30:33]
	s_waitcnt lgkmcnt(0)
	v_mfma_f32_16x16x32_f16 v[46:49], v[42:45], v[2:5], v[34:37]
	s_nop 2
	ds_read_b128 v[34:37], v115 offset:4096
	v_mfma_f32_16x16x32_f16 v[42:45], v[110:113], v[2:5], v[38:41]
	ds_read_b128 v[110:113], v115 offset:6144
	s_waitcnt lgkmcnt(0)
	v_mfma_f32_16x16x32_f16 v[38:41], v[34:37], v[2:5], v[102:105]
	v_mfma_f32_16x16x32_f16 v[34:37], v[110:113], v[2:5], v[106:109]
	s_setprio 0
	s_cbranch_scc1 .LBB2_12
	v_cndmask_b32_e64 v69, v46, v100, s[2:3]
	v_cndmask_b32_e64 v46, v69, v46, s[4:5]
	v_cndmask_b32_e64 v47, v100, v47, s[4:5]
	v_cndmask_b32_e64 v48, v48, v100, s[6:7]
	v_cndmask_b32_e64 v49, v49, v100, s[8:9]
	v_cndmask_b32_e64 v42, v42, v100, s[10:11]
	v_cndmask_b32_e64 v43, v43, v100, s[12:13]
	v_cndmask_b32_e64 v44, v44, v100, s[14:15]
	v_cndmask_b32_e64 v45, v45, v100, s[16:17]
	v_cndmask_b32_e64 v38, v38, v100, s[18:19]
	v_cndmask_b32_e64 v39, v39, v100, s[20:21]
	v_cndmask_b32_e64 v40, v40, v100, s[22:23]
	v_cndmask_b32_e64 v41, v41, v100, s[24:25]
	v_cndmask_b32_e64 v34, v34, v100, s[26:27]
	v_cndmask_b32_e64 v35, v35, v100, s[28:29]
	v_cndmask_b32_e64 v36, v36, v100, s[30:31]
	v_cndmask_b32_e64 v37, v37, v100, s[34:35]
